# A/B of the static priority raise: waves 0-3 (the other half) at s_setprio 1 during the attention phase instead of waves 4-7
# baseline (speedup 1.0000x reference)
.LBB0_259:
	v_readlane_b32 s100, v252, 5
	s_cmp_lt_u32 s100, 4
	s_cbranch_scc0 .Lattn_prio_done
	s_setprio 1
